# h-table L2 prefetch spread over all blocks of an XCD (807-line slices)
# speedup vs baseline: 1.0039x; 1.0039x over previous
.LBB2_99:
	s_movk_i32 s2, 0x190
	v_mov_b32_e32 v2, 0x10000
	v_cmp_gt_u32_e32 vcc, s2, v0
	v_lshl_or_b32 v35, v0, 2, v2
	v_mov_b32_e32 v36, 0
	v_mov_b32_e32 v37, 0
	s_waitcnt lgkmcnt(0)
	s_barrier
	s_mul_i32 s84, s83, 0x327
	v_min_u32_e32 v112, 0x326, v0
	v_add_u32_e32 v112, s84, v112
	v_min_u32_e32 v112, 0x61a7, v112
	v_lshlrev_b32_e32 v112, 7, v112
	global_load_dword v112, v112, s[56:57]
	s_and_saveexec_b64 s[2:3], vcc
	ds_read_b32 v37, v35
	s_or_b64 exec, exec, s[2:3]
	s_and_saveexec_b64 s[2:3], vcc
	ds_read_b32 v36, v35 offset:1600
	s_or_b64 exec, exec, s[2:3]
	v_mov_b32_e32 v38, 0
	v_mov_b32_e32 v39, 0
	s_and_saveexec_b64 s[2:3], vcc
	ds_read_b32 v39, v35 offset:3200
	s_or_b64 exec, exec, s[2:3]
	s_and_saveexec_b64 s[2:3], vcc
	ds_read_b32 v38, v35 offset:4800
	s_or_b64 exec, exec, s[2:3]
	v_mov_b32_e32 v40, 0
	v_mov_b32_e32 v41, 0
	s_and_saveexec_b64 s[2:3], vcc
	ds_read_b32 v41, v35 offset:6400
	s_or_b64 exec, exec, s[2:3]
	s_and_saveexec_b64 s[2:3], vcc
	ds_read_b32 v40, v35 offset:8000
	s_or_b64 exec, exec, s[2:3]
	v_mov_b32_e32 v43, 0
	v_mov_b32_e32 v44, 0
	s_and_saveexec_b64 s[2:3], vcc
	ds_read_b32 v44, v35 offset:9600
	s_or_b64 exec, exec, s[2:3]
	s_and_saveexec_b64 s[2:3], vcc
	ds_read_b32 v43, v35 offset:11200
	s_or_b64 exec, exec, s[2:3]
	v_mov_b32_e32 v46, 0
	v_mov_b32_e32 v47, 0
	s_and_saveexec_b64 s[2:3], vcc
	ds_read_b32 v47, v35 offset:12800
	s_or_b64 exec, exec, s[2:3]
	s_and_saveexec_b64 s[2:3], vcc
	ds_read_b32 v46, v35 offset:14400
	s_or_b64 exec, exec, s[2:3]
	v_mov_b32_e32 v53, 0
	v_mov_b32_e32 v54, 0
	s_and_saveexec_b64 s[2:3], vcc
	ds_read_b32 v54, v35 offset:16000
	s_or_b64 exec, exec, s[2:3]
	s_and_saveexec_b64 s[2:3], vcc
	ds_read_b32 v53, v35 offset:17600
	s_or_b64 exec, exec, s[2:3]
	v_mov_b32_e32 v55, 0
	v_mov_b32_e32 v56, 0
	s_and_saveexec_b64 s[2:3], vcc
	ds_read_b32 v56, v35 offset:19200
	s_or_b64 exec, exec, s[2:3]
	s_and_saveexec_b64 s[2:3], vcc
	ds_read_b32 v55, v35 offset:20800
	s_or_b64 exec, exec, s[2:3]
	v_mov_b32_e32 v2, 0
	v_mov_b32_e32 v57, 0
	s_and_saveexec_b64 s[2:3], vcc
	ds_read_b32 v57, v35 offset:22400
	s_or_b64 exec, exec, s[2:3]
	s_and_saveexec_b64 s[2:3], vcc
	ds_read_b32 v2, v35 offset:24000
	s_or_b64 exec, exec, s[2:3]
	s_waitcnt lgkmcnt(0)
	v_add_u32_e32 v3, v36, v37
	v_add3_u32 v3, v39, v3, v38
	v_add3_u32 v3, v41, v3, v40
	v_add3_u32 v3, v44, v3, v43
	v_add3_u32 v3, v47, v3, v46
	v_add3_u32 v3, v54, v3, v53
	v_add3_u32 v3, v56, v3, v55
	v_add3_u32 v58, v57, v3, v2
	v_mbcnt_lo_u32_b32 v2, -1, 0
	v_mbcnt_hi_u32_b32 v51, -1, v2
	v_and_b32_e32 v52, 64, v51
	v_mov_b32_e32 v59, v58
	s_nop 1
	v_add_u32_dpp v59, v59, v59 row_shr:1 row_mask:0xf bank_mask:0xf
	s_nop 1
	v_add_u32_dpp v59, v59, v59 row_shr:2 row_mask:0xf bank_mask:0xf
	s_nop 1
	v_add_u32_dpp v59, v59, v59 row_shr:4 row_mask:0xf bank_mask:0xf
	s_nop 1
	v_add_u32_dpp v59, v59, v59 row_shr:8 row_mask:0xf bank_mask:0xf
	s_nop 1
	v_add_u32_dpp v59, v59, v59 row_bcast:15 row_mask:0xa bank_mask:0xf
	s_nop 1
	v_add_u32_dpp v59, v59, v59 row_bcast:31 row_mask:0xc bank_mask:0xf
	v_cmp_eq_u32_e64 s[2:3], 63, v45
	s_and_saveexec_b64 s[4:5], s[2:3]
	s_xor_b64 s[2:3], exec, s[4:5]
	v_mov_b32_e32 v2, 0x17cf0
	v_lshl_add_u32 v2, v6, 2, v2
	ds_write_b32 v2, v59
	s_or_b64 exec, exec, s[2:3]
	v_mov_b32_e32 v2, 0x17cf0
	v_mov_b32_e32 v3, 0x17d00
	s_waitcnt lgkmcnt(0)
	s_barrier
	ds_read_b128 v[14:17], v2
	ds_read_b128 v[6:9], v3
	v_mov_b32_e32 v2, 0x17d10
	v_mov_b32_e32 v3, 0x17d20
	ds_read_b128 v[10:13], v2
	ds_read_b128 v[2:5], v3
	s_and_saveexec_b64 s[2:3], vcc
	s_cbranch_execz .LBB2_135
	v_cmp_lt_u32_e32 vcc, 63, v0
	s_movk_i32 s4, 0x7f
	v_sub_u32_e32 v58, v59, v58
	s_waitcnt lgkmcnt(3)
	v_cndmask_b32_e32 v60, 0, v14, vcc
	v_cmp_lt_u32_e32 vcc, s4, v0
	s_movk_i32 s4, 0xbf
	s_nop 0
	v_cndmask_b32_e32 v59, 0, v15, vcc
	v_cmp_lt_u32_e32 vcc, s4, v0
	s_movk_i32 s4, 0xff
	v_add3_u32 v58, v60, v58, v59
	v_cndmask_b32_e32 v59, 0, v16, vcc
	v_cmp_lt_u32_e32 vcc, s4, v0
	s_movk_i32 s4, 0x13f
	s_nop 0
	v_cndmask_b32_e32 v60, 0, v17, vcc
	v_cmp_lt_u32_e32 vcc, s4, v0
	s_movk_i32 s4, 0x17f
	v_add3_u32 v58, v58, v59, v60
	s_waitcnt lgkmcnt(2)
	v_cndmask_b32_e32 v59, 0, v6, vcc
	v_cmp_lt_u32_e32 vcc, s4, v0
	s_nop 1
	v_cndmask_b32_e32 v60, 0, v7, vcc
	v_add3_u32 v58, v58, v59, v60
	v_add_u32_e32 v37, v37, v58
	v_add_u32_e32 v36, v36, v37
	ds_write_b32 v35, v36 offset:3200
	v_add_u32_e32 v36, v39, v36
	ds_write_b32 v35, v36 offset:4800
	v_add_u32_e32 v36, v38, v36
	ds_write_b32 v35, v36 offset:6400
	v_add_u32_e32 v36, v41, v36
	ds_write_b32 v35, v36 offset:8000
	v_add_u32_e32 v36, v40, v36
	ds_write_b32 v35, v36 offset:9600
	v_add_u32_e32 v36, v44, v36
	ds_write_b32 v35, v36 offset:11200
	v_add_u32_e32 v36, v43, v36
	ds_write_b32 v35, v36 offset:12800
	v_add_u32_e32 v36, v47, v36
	ds_write_b32 v35, v36 offset:14400
	v_add_u32_e32 v36, v46, v36
	ds_write_b32 v35, v36 offset:16000
	v_add_u32_e32 v36, v54, v36
	ds_write_b32 v35, v36 offset:17600
	v_add_u32_e32 v36, v53, v36
	ds_write_b32 v35, v36 offset:19200
	v_add_u32_e32 v36, v56, v36
	ds_write_b32 v35, v36 offset:20800
	v_add_u32_e32 v36, v55, v36
	ds_write_b32 v35, v36 offset:22400
	v_add_u32_e32 v36, v57, v36
	ds_write_b32 v35, v58
	ds_write_b32 v35, v37 offset:1600
	ds_write_b32 v35, v36 offset:24000
	v_mov_b32_e32 v35, 0x16e00
	v_lshl_add_u32 v35, v0, 2, v35
	ds_write_b32 v35, v58
